# s18_deep
# baseline (speedup 1.0000x reference)
.LBB2_3:
	s_load_dwordx8 s[12:19], s[0:1], 0x10
	v_lshrrev_b32_e32 v2, 2, v0
	s_lshr_b32 s5, s21, 8
	v_sub_u32_e32 v2, 0, v2
	v_and_b32_e32 v102, 15, v0
	v_bitop3_b32 v2, v120, v2, 3 bitop3:0x78
	s_mul_i32 s25, s5, 0x60
	s_and_b32 s2, s22, 3
	v_lshlrev_b32_e32 v98, 4, v2
	v_or_b32_e32 v2, s25, v102
	v_mov_b32_e32 v50, 0
	s_mov_b32 s3, 0
	v_lshlrev_b32_e32 v99, 6, v2
	s_lshl_b32 s6, s2, 12
	s_mov_b32 s7, 32
	v_mov_b32_e32 v51, v50
	v_mov_b32_e32 v52, v50
	v_mov_b32_e32 v53, v50
	v_mov_b32_e32 v74, v50
	v_mov_b32_e32 v75, v50
	v_mov_b32_e32 v76, v50
	v_mov_b32_e32 v77, v50
	v_mov_b32_e32 v6, v50
	v_mov_b32_e32 v7, v50
	v_mov_b32_e32 v8, v50
	v_mov_b32_e32 v9, v50
	v_mov_b32_e32 v26, v50
	v_mov_b32_e32 v27, v50
	v_mov_b32_e32 v28, v50
	v_mov_b32_e32 v29, v50
	v_mov_b32_e32 v54, v50
	v_mov_b32_e32 v55, v50
	v_mov_b32_e32 v56, v50
	v_mov_b32_e32 v57, v50
	v_mov_b32_e32 v86, v50
	v_mov_b32_e32 v87, v50
	v_mov_b32_e32 v88, v50
	v_mov_b32_e32 v89, v50
	v_mov_b32_e32 v18, v50
	v_mov_b32_e32 v19, v50
	v_mov_b32_e32 v20, v50
	v_mov_b32_e32 v21, v50
	v_mov_b32_e32 v42, v50
	v_mov_b32_e32 v43, v50
	v_mov_b32_e32 v44, v50
	v_mov_b32_e32 v45, v50
	v_mov_b32_e32 v66, v50
	v_mov_b32_e32 v67, v50
	v_mov_b32_e32 v68, v50
	v_mov_b32_e32 v69, v50
	v_mov_b32_e32 v90, v50
	v_mov_b32_e32 v91, v50
	v_mov_b32_e32 v92, v50
	v_mov_b32_e32 v93, v50
	v_mov_b32_e32 v22, v50
	v_mov_b32_e32 v23, v50
	v_mov_b32_e32 v24, v50
	v_mov_b32_e32 v25, v50
	v_mov_b32_e32 v46, v50
	v_mov_b32_e32 v47, v50
	v_mov_b32_e32 v48, v50
	v_mov_b32_e32 v49, v50
	v_mov_b32_e32 v70, v50
	v_mov_b32_e32 v71, v50
	v_mov_b32_e32 v72, v50
	v_mov_b32_e32 v73, v50
	v_mov_b32_e32 v94, v50
	v_mov_b32_e32 v95, v50
	v_mov_b32_e32 v96, v50
	v_mov_b32_e32 v97, v50
	v_mov_b32_e32 v38, v50
	v_mov_b32_e32 v39, v50
	v_mov_b32_e32 v40, v50
	v_mov_b32_e32 v41, v50
	v_mov_b32_e32 v14, v50
	v_mov_b32_e32 v15, v50
	v_mov_b32_e32 v16, v50
	v_mov_b32_e32 v17, v50
	v_mov_b32_e32 v82, v50
	v_mov_b32_e32 v83, v50
	v_mov_b32_e32 v84, v50
	v_mov_b32_e32 v85, v50
	v_mov_b32_e32 v58, v50
	v_mov_b32_e32 v59, v50
	v_mov_b32_e32 v60, v50
	v_mov_b32_e32 v61, v50
	v_mov_b32_e32 v30, v50
	v_mov_b32_e32 v31, v50
	v_mov_b32_e32 v32, v50
	v_mov_b32_e32 v33, v50
	v_mov_b32_e32 v10, v50
	v_mov_b32_e32 v11, v50
	v_mov_b32_e32 v12, v50
	v_mov_b32_e32 v13, v50
	v_mov_b32_e32 v78, v50
	v_mov_b32_e32 v79, v50
	v_mov_b32_e32 v80, v50
	v_mov_b32_e32 v81, v50
	v_mov_b32_e32 v62, v50
	v_mov_b32_e32 v63, v50
	v_mov_b32_e32 v64, v50
	v_mov_b32_e32 v65, v50
	v_mov_b32_e32 v34, v50
	v_mov_b32_e32 v35, v50
	v_mov_b32_e32 v36, v50
	v_mov_b32_e32 v37, v50
	v_mov_b32_e32 v2, v50
	v_mov_b32_e32 v3, v50
	v_mov_b32_e32 v4, v50
	v_mov_b32_e32 v5, v50
	v_lshlrev_b32_e32 v100, 6, v102
	v_add_u32_e32 v99, v99, v98
	v_add3_u32 v100, s6, v100, v98
	s_barrier
	ds_read_b128 v[104:107], v100 offset:12288
	ds_read_b128 v[108:111], v100 offset:13312
	ds_read_b128 v[112:115], v100 offset:14336
	ds_read_b128 v[116:119], v100 offset:15360
	ds_read_b128 v[122:125], v99
	ds_read_b128 v[126:129], v99 offset:1024
	ds_read_b128 v[130:133], v99 offset:2048
	ds_read_b128 v[134:137], v99 offset:3072
	ds_read_b128 v[138:141], v99 offset:4096
	ds_read_b128 v[142:145], v99 offset:5120
	s_mov_b32 s3, 1
	s_mov_b32 s7, 16
	s_waitcnt lgkmcnt(0)
.Lg0_cloop:
	s_mul_i32 s8, s3, 0x7000
	s_barrier
	v_add_u32_e32 v103, s8, v100
	v_add_u32_e32 v101, s8, v99
	ds_read_b128 v[146:149], v103 offset:12288
	ds_read_b128 v[150:153], v103 offset:13312
	ds_read_b128 v[154:157], v103 offset:14336
	ds_read_b128 v[158:161], v103 offset:15360
	ds_read_b128 v[162:165], v101 offset:5120
	v_mfma_f32_16x16x32_f16 v[94:97], v[122:125], v[104:107], v[94:97]
	s_add_i32 s8, s3, 1
	s_cmp_lg_u32 s3, 4
	s_cselect_b32 s3, s8, 0
	v_mfma_f32_16x16x32_f16 v[70:73], v[122:125], v[108:111], v[70:73]
	v_mfma_f32_16x16x32_f16 v[46:49], v[122:125], v[112:115], v[46:49]
	v_mfma_f32_16x16x32_f16 v[22:25], v[122:125], v[116:119], v[22:25]
	ds_read_b128 v[122:125], v101
	v_mfma_f32_16x16x32_f16 v[90:93], v[126:129], v[104:107], v[90:93]
	v_mfma_f32_16x16x32_f16 v[66:69], v[126:129], v[108:111], v[66:69]
	v_mfma_f32_16x16x32_f16 v[42:45], v[126:129], v[112:115], v[42:45]
	v_mfma_f32_16x16x32_f16 v[18:21], v[126:129], v[116:119], v[18:21]
	ds_read_b128 v[126:129], v101 offset:1024
	v_mfma_f32_16x16x32_f16 v[86:89], v[130:133], v[104:107], v[86:89]
	v_mfma_f32_16x16x32_f16 v[54:57], v[130:133], v[108:111], v[54:57]
	v_mfma_f32_16x16x32_f16 v[26:29], v[130:133], v[112:115], v[26:29]
	v_mfma_f32_16x16x32_f16 v[6:9], v[130:133], v[116:119], v[6:9]
	ds_read_b128 v[130:133], v101 offset:2048
	v_mfma_f32_16x16x32_f16 v[74:77], v[134:137], v[104:107], v[74:77]
	v_mfma_f32_16x16x32_f16 v[50:53], v[134:137], v[108:111], v[50:53]
	v_mfma_f32_16x16x32_f16 v[38:41], v[134:137], v[112:115], v[38:41]
	v_mfma_f32_16x16x32_f16 v[14:17], v[134:137], v[116:119], v[14:17]
	ds_read_b128 v[134:137], v101 offset:3072
	v_mfma_f32_16x16x32_f16 v[82:85], v[138:141], v[104:107], v[82:85]
	v_mfma_f32_16x16x32_f16 v[58:61], v[138:141], v[108:111], v[58:61]
	v_mfma_f32_16x16x32_f16 v[30:33], v[138:141], v[112:115], v[30:33]
	v_mfma_f32_16x16x32_f16 v[10:13], v[138:141], v[116:119], v[10:13]
	ds_read_b128 v[138:141], v101 offset:4096
	v_mfma_f32_16x16x32_f16 v[78:81], v[142:145], v[104:107], v[78:81]
	v_mfma_f32_16x16x32_f16 v[62:65], v[142:145], v[108:111], v[62:65]
	v_mfma_f32_16x16x32_f16 v[34:37], v[142:145], v[112:115], v[34:37]
	v_mfma_f32_16x16x32_f16 v[2:5], v[142:145], v[116:119], v[2:5]
	s_waitcnt lgkmcnt(0)
	s_mul_i32 s8, s3, 0x7000
	s_barrier
	v_add_u32_e32 v103, s8, v100
	v_add_u32_e32 v101, s8, v99
	ds_read_b128 v[104:107], v103 offset:12288
	ds_read_b128 v[108:111], v103 offset:13312
	ds_read_b128 v[112:115], v103 offset:14336
	ds_read_b128 v[116:119], v103 offset:15360
	ds_read_b128 v[142:145], v101 offset:5120
	v_mfma_f32_16x16x32_f16 v[94:97], v[122:125], v[146:149], v[94:97]
	s_add_i32 s8, s3, 1
	s_cmp_lg_u32 s3, 4
	s_cselect_b32 s3, s8, 0
	v_mfma_f32_16x16x32_f16 v[70:73], v[122:125], v[150:153], v[70:73]
	v_mfma_f32_16x16x32_f16 v[46:49], v[122:125], v[154:157], v[46:49]
	v_mfma_f32_16x16x32_f16 v[22:25], v[122:125], v[158:161], v[22:25]
	ds_read_b128 v[122:125], v101
	v_mfma_f32_16x16x32_f16 v[90:93], v[126:129], v[146:149], v[90:93]
	v_mfma_f32_16x16x32_f16 v[66:69], v[126:129], v[150:153], v[66:69]
	v_mfma_f32_16x16x32_f16 v[42:45], v[126:129], v[154:157], v[42:45]
	v_mfma_f32_16x16x32_f16 v[18:21], v[126:129], v[158:161], v[18:21]
	ds_read_b128 v[126:129], v101 offset:1024
	v_mfma_f32_16x16x32_f16 v[86:89], v[130:133], v[146:149], v[86:89]
	v_mfma_f32_16x16x32_f16 v[54:57], v[130:133], v[150:153], v[54:57]
	v_mfma_f32_16x16x32_f16 v[26:29], v[130:133], v[154:157], v[26:29]
	v_mfma_f32_16x16x32_f16 v[6:9], v[130:133], v[158:161], v[6:9]
	ds_read_b128 v[130:133], v101 offset:2048
	v_mfma_f32_16x16x32_f16 v[74:77], v[134:137], v[146:149], v[74:77]
	v_mfma_f32_16x16x32_f16 v[50:53], v[134:137], v[150:153], v[50:53]
	v_mfma_f32_16x16x32_f16 v[38:41], v[134:137], v[154:157], v[38:41]
	v_mfma_f32_16x16x32_f16 v[14:17], v[134:137], v[158:161], v[14:17]
	ds_read_b128 v[134:137], v101 offset:3072
	v_mfma_f32_16x16x32_f16 v[82:85], v[138:141], v[146:149], v[82:85]
	v_mfma_f32_16x16x32_f16 v[58:61], v[138:141], v[150:153], v[58:61]
	v_mfma_f32_16x16x32_f16 v[30:33], v[138:141], v[154:157], v[30:33]
	v_mfma_f32_16x16x32_f16 v[10:13], v[138:141], v[158:161], v[10:13]
	ds_read_b128 v[138:141], v101 offset:4096
	v_mfma_f32_16x16x32_f16 v[78:81], v[162:165], v[146:149], v[78:81]
	v_mfma_f32_16x16x32_f16 v[62:65], v[162:165], v[150:153], v[62:65]
	v_mfma_f32_16x16x32_f16 v[34:37], v[162:165], v[154:157], v[34:37]
	v_mfma_f32_16x16x32_f16 v[2:5], v[162:165], v[158:161], v[2:5]
	s_waitcnt lgkmcnt(0)
	s_add_i32 s7, s7, -1
	s_cmp_eq_u32 s7, 0
	s_cbranch_scc0 .Lg0_cloop
	s_barrier
	s_mul_i32 s24, s22, 0x3400
	s_lshl_b32 s28, s2, 6
	s_add_i32 s29, s20, s28
	s_and_b32 s30, s29, 0x7ff
	v_add_u32_e32 v98, s30, v102
	v_lshlrev_b32_e32 v98, 8, v98
	v_lshl_add_u32 v98, v120, 4, v98
	v_add_u32_e32 v99, 0x1000, v98
	v_add_u32_e32 v100, 0x2000, v98
	v_add_u32_e32 v101, 0x3000, v98
	v_mul_u32_u24_e32 v103, 0xd0, v102
	v_lshl_add_u32 v103, v120, 3, v103
	v_add_u32_e32 v103, s24, v103
	v_lshrrev_b32_e32 v0, 2, v1
	v_and_b32_e32 v1, 3, v1
	v_mul_u32_u24_e32 v102, 0xd0, v0
	v_lshl_add_u32 v102, v1, 4, v102
	v_add_u32_e32 v102, s24, v102
	v_lshlrev_b32_e32 v0, 11, v0
	v_lshl_add_u32 v0, v1, 4, v0
	s_lshl_b32 s31, s5, 7
	s_add_i32 s35, s31, 0
	s_and_b32 s35, s35, 0xff
	s_add_u32 s36, s12, s35
	s_addc_u32 s37, s13, 0
	s_add_i32 s35, s31, 64
	s_and_b32 s35, s35, 0xff
	s_add_u32 s38, s12, s35
	s_addc_u32 s39, s13, 0
	s_add_i32 s35, s31, 128
	s_and_b32 s35, s35, 0xff
	s_add_u32 s40, s12, s35
	s_addc_u32 s41, s13, 0
	s_add_i32 s35, s31, 192
	s_and_b32 s35, s35, 0xff
	s_add_u32 s42, s12, s35
	s_addc_u32 s43, s13, 0
	global_load_dwordx4 v[104:107], v98, s[36:37]
	global_load_dwordx4 v[108:111], v98, s[38:39]
	global_load_dwordx4 v[112:115], v98, s[40:41]
	global_load_dwordx4 v[116:119], v98, s[42:43]
	global_load_dwordx4 v[120:123], v99, s[36:37]
	global_load_dwordx4 v[124:127], v99, s[38:39]
	global_load_dwordx4 v[128:131], v99, s[40:41]
	global_load_dwordx4 v[132:135], v99, s[42:43]
	global_load_dwordx4 v[136:139], v100, s[36:37]
	global_load_dwordx4 v[140:143], v100, s[38:39]
	global_load_dwordx4 v[144:147], v100, s[40:41]
	global_load_dwordx4 v[148:151], v100, s[42:43]
	global_load_dwordx4 v[152:155], v101, s[36:37]
	global_load_dwordx4 v[156:159], v101, s[38:39]
	global_load_dwordx4 v[160:163], v101, s[40:41]
	global_load_dwordx4 v[164:167], v101, s[42:43]
	s_add_i32 s34, s25, s23
	s_sub_i32 s32, 0x400, s34
	s_ashr_i32 s32, s32, 4
	s_max_i32 s32, s32, 0
	s_min_i32 s32, s32, 6
	s_sub_i32 s33, 0x800, s34
	s_ashr_i32 s33, s33, 4
	s_max_i32 s33, s33, 0
	s_min_i32 s33, s33, 6
	s_cmp_le_u32 s33, 5
	s_cbranch_scc1 .Lepi_v5
	s_waitcnt vmcnt(0)
	s_cmp_lg_u32 s32, 6
	s_cbranch_scc1 .Lepi_r5
	v_mul_f32_e32 v104, 0x3e38aa3b, v104
	v_mul_f32_e32 v105, 0x3e38aa3b, v105
	v_mul_f32_e32 v106, 0x3e38aa3b, v106
	v_mul_f32_e32 v107, 0x3e38aa3b, v107
	v_mul_f32_e32 v108, 0x3e38aa3b, v108
	v_mul_f32_e32 v109, 0x3e38aa3b, v109
	v_mul_f32_e32 v110, 0x3e38aa3b, v110
	v_mul_f32_e32 v111, 0x3e38aa3b, v111
	v_mul_f32_e32 v112, 0x3e38aa3b, v112
	v_mul_f32_e32 v113, 0x3e38aa3b, v113
	v_mul_f32_e32 v114, 0x3e38aa3b, v114
	v_mul_f32_e32 v115, 0x3e38aa3b, v115
	v_mul_f32_e32 v116, 0x3e38aa3b, v116
	v_mul_f32_e32 v117, 0x3e38aa3b, v117
	v_mul_f32_e32 v118, 0x3e38aa3b, v118
	v_mul_f32_e32 v119, 0x3e38aa3b, v119
	v_mul_f32_e32 v120, 0x3e38aa3b, v120
	v_mul_f32_e32 v121, 0x3e38aa3b, v121
	v_mul_f32_e32 v122, 0x3e38aa3b, v122
	v_mul_f32_e32 v123, 0x3e38aa3b, v123
	v_mul_f32_e32 v124, 0x3e38aa3b, v124
	v_mul_f32_e32 v125, 0x3e38aa3b, v125
	v_mul_f32_e32 v126, 0x3e38aa3b, v126
	v_mul_f32_e32 v127, 0x3e38aa3b, v127
	v_mul_f32_e32 v128, 0x3e38aa3b, v128
	v_mul_f32_e32 v129, 0x3e38aa3b, v129
	v_mul_f32_e32 v130, 0x3e38aa3b, v130
	v_mul_f32_e32 v131, 0x3e38aa3b, v131
	v_mul_f32_e32 v132, 0x3e38aa3b, v132
	v_mul_f32_e32 v133, 0x3e38aa3b, v133
	v_mul_f32_e32 v134, 0x3e38aa3b, v134
	v_mul_f32_e32 v135, 0x3e38aa3b, v135
	v_mul_f32_e32 v136, 0x3e38aa3b, v136
	v_mul_f32_e32 v137, 0x3e38aa3b, v137
	v_mul_f32_e32 v138, 0x3e38aa3b, v138
	v_mul_f32_e32 v139, 0x3e38aa3b, v139
	v_mul_f32_e32 v140, 0x3e38aa3b, v140
	v_mul_f32_e32 v141, 0x3e38aa3b, v141
	v_mul_f32_e32 v142, 0x3e38aa3b, v142
	v_mul_f32_e32 v143, 0x3e38aa3b, v143
	v_mul_f32_e32 v144, 0x3e38aa3b, v144
	v_mul_f32_e32 v145, 0x3e38aa3b, v145
	v_mul_f32_e32 v146, 0x3e38aa3b, v146
	v_mul_f32_e32 v147, 0x3e38aa3b, v147
	v_mul_f32_e32 v148, 0x3e38aa3b, v148
	v_mul_f32_e32 v149, 0x3e38aa3b, v149
	v_mul_f32_e32 v150, 0x3e38aa3b, v150
	v_mul_f32_e32 v151, 0x3e38aa3b, v151
	v_mul_f32_e32 v152, 0x3e38aa3b, v152
	v_mul_f32_e32 v153, 0x3e38aa3b, v153
	v_mul_f32_e32 v154, 0x3e38aa3b, v154
	v_mul_f32_e32 v155, 0x3e38aa3b, v155
	v_mul_f32_e32 v156, 0x3e38aa3b, v156
	v_mul_f32_e32 v157, 0x3e38aa3b, v157
	v_mul_f32_e32 v158, 0x3e38aa3b, v158
	v_mul_f32_e32 v159, 0x3e38aa3b, v159
	v_mul_f32_e32 v160, 0x3e38aa3b, v160
	v_mul_f32_e32 v161, 0x3e38aa3b, v161
	v_mul_f32_e32 v162, 0x3e38aa3b, v162
	v_mul_f32_e32 v163, 0x3e38aa3b, v163
	v_mul_f32_e32 v164, 0x3e38aa3b, v164
	v_mul_f32_e32 v165, 0x3e38aa3b, v165
	v_mul_f32_e32 v166, 0x3e38aa3b, v166
	v_mul_f32_e32 v167, 0x3e38aa3b, v167

.LBB2_6:
	s_load_dwordx4 s[0:3], s[0:1], 0x0
	s_add_i32 s9, s22, -8
	s_mov_b32 s28, s23
	s_mov_b32 s29, s20
	v_and_b32_e32 v1, 63, v0
	v_bfe_u32 v3, v0, 4, 2
	v_lshrrev_b32_e32 v2, 2, v1
	v_sub_u32_e32 v3, 0, v3
	v_and_b32_e32 v3, 3, v3
	v_and_b32_e32 v4, 3, v1
	v_xor_b32_e32 v3, v3, v4
	v_lshlrev_b32_e32 v3, 4, v3
	v_lshl_or_b32 v2, v2, 6, v3
	s_lshl_b32 s4, s9, 4
	s_add_i32 s5, s28, s4
	s_lshl_b32 s5, s5, 6
	s_add_i32 s6, s29, s4
	s_lshl_b32 s6, s6, 6
	s_lshl_b32 s8, s9, 10
	s_waitcnt lgkmcnt(0)
	s_add_u32 s10, s0, s5
	s_addc_u32 s11, s1, 0
	s_add_u32 s12, s10, 0x1000
	s_addc_u32 s13, s11, 0
	s_add_u32 s14, s12, 0x1000
	s_addc_u32 s15, s13, 0
	s_add_u32 s16, s2, s6
	s_addc_u32 s17, s3, 0
	s_add_u32 s18, s16, 0x1000
	s_addc_u32 s19, s17, 0
	s_add_u32 s24, s18, 0x1000
	s_addc_u32 s25, s19, 0
	s_add_u32 s26, s24, 0x1000
	s_addc_u32 s27, s25, 0
	v_mov_b32_e32 v5, v2
	v_mov_b32_e32 v6, v2
	s_add_i32 m0, s8, 0
	s_nop 0
	global_load_lds_dwordx4 v5, s[10:11]
	s_add_i32 m0, s8, 4096
	s_nop 0
	global_load_lds_dwordx4 v5, s[12:13]
	s_add_i32 m0, s8, 8192
	s_nop 0
	global_load_lds_dwordx4 v5, s[14:15]
	s_add_i32 m0, s8, 12288
	s_nop 0
	global_load_lds_dwordx4 v6, s[16:17]
	s_add_i32 m0, s8, 16384
	s_nop 0
	global_load_lds_dwordx4 v6, s[18:19]
	s_add_i32 m0, s8, 20480
	s_nop 0
	global_load_lds_dwordx4 v6, s[24:25]
	s_add_i32 m0, s8, 24576
	s_nop 0
	global_load_lds_dwordx4 v6, s[26:27]
	v_add_u32_e32 v5, 196608, v5
	v_add_u32_e32 v6, 262144, v6
	s_add_i32 m0, s8, 28672
	s_nop 0
	global_load_lds_dwordx4 v5, s[10:11]
	s_add_i32 m0, s8, 32768
	s_nop 0
	global_load_lds_dwordx4 v5, s[12:13]
	s_add_i32 m0, s8, 36864
	s_nop 0
	global_load_lds_dwordx4 v5, s[14:15]
	s_add_i32 m0, s8, 40960
	s_nop 0
	global_load_lds_dwordx4 v6, s[16:17]
	s_add_i32 m0, s8, 45056
	s_nop 0
	global_load_lds_dwordx4 v6, s[18:19]
	s_add_i32 m0, s8, 49152
	s_nop 0
	global_load_lds_dwordx4 v6, s[24:25]
	s_add_i32 m0, s8, 53248
	s_nop 0
	global_load_lds_dwordx4 v6, s[26:27]
	v_add_u32_e32 v5, 196608, v5
	v_add_u32_e32 v6, 262144, v6
	s_add_i32 m0, s8, 57344
	s_nop 0
	global_load_lds_dwordx4 v5, s[10:11]
	s_add_i32 m0, s8, 61440
	s_nop 0
	global_load_lds_dwordx4 v5, s[12:13]
	s_add_i32 m0, s8, 65536
	s_nop 0
	global_load_lds_dwordx4 v5, s[14:15]
	s_add_i32 m0, s8, 69632
	s_nop 0
	global_load_lds_dwordx4 v6, s[16:17]
	s_add_i32 m0, s8, 73728
	s_nop 0
	global_load_lds_dwordx4 v6, s[18:19]
	s_add_i32 m0, s8, 77824
	s_nop 0
	global_load_lds_dwordx4 v6, s[24:25]
	s_add_i32 m0, s8, 81920
	s_nop 0
	global_load_lds_dwordx4 v6, s[26:27]
	v_add_u32_e32 v5, 196608, v5
	v_add_u32_e32 v6, 262144, v6
	s_add_i32 m0, s8, 86016
	s_nop 0
	global_load_lds_dwordx4 v5, s[10:11]
	s_add_i32 m0, s8, 90112
	s_nop 0
	global_load_lds_dwordx4 v5, s[12:13]
	s_add_i32 m0, s8, 94208
	s_nop 0
	global_load_lds_dwordx4 v5, s[14:15]
	s_add_i32 m0, s8, 98304
	s_nop 0
	global_load_lds_dwordx4 v6, s[16:17]
	s_add_i32 m0, s8, 102400
	s_nop 0
	global_load_lds_dwordx4 v6, s[18:19]
	s_add_i32 m0, s8, 106496
	s_nop 0
	global_load_lds_dwordx4 v6, s[24:25]
	s_add_i32 m0, s8, 110592
	s_nop 0
	global_load_lds_dwordx4 v6, s[26:27]
	v_add_u32_e32 v5, 196608, v5
	v_add_u32_e32 v6, 262144, v6
	s_add_i32 m0, s8, 114688
	s_nop 0
	global_load_lds_dwordx4 v5, s[10:11]
	s_add_i32 m0, s8, 118784
	s_nop 0
	global_load_lds_dwordx4 v5, s[12:13]
	s_add_i32 m0, s8, 122880
	s_nop 0
	global_load_lds_dwordx4 v5, s[14:15]
	s_add_i32 m0, s8, 126976
	s_nop 0
	global_load_lds_dwordx4 v6, s[16:17]
	s_add_i32 m0, s8, 131072
	s_nop 0
	global_load_lds_dwordx4 v6, s[18:19]
	s_add_i32 m0, s8, 135168
	s_nop 0
	global_load_lds_dwordx4 v6, s[24:25]
	s_add_i32 m0, s8, 139264
	s_nop 0
	global_load_lds_dwordx4 v6, s[26:27]
	v_add_u32_e32 v5, 196608, v5
	v_add_u32_e32 v6, 262144, v6
	s_waitcnt vmcnt(28)
	s_barrier
	s_mov_b32 s29, 0
	s_mov_b32 s30, 27
.Lg0_ploop:
	s_mul_i32 s28, s29, 28672
	s_add_i32 s28, s28, s8
	s_waitcnt vmcnt(21)
	s_barrier
	s_mov_b32 m0, s28
	s_add_i32 s28, s28, 0x1000
	global_load_lds_dwordx4 v5, s[10:11]
	s_mov_b32 m0, s28
	s_add_i32 s28, s28, 0x1000
	global_load_lds_dwordx4 v5, s[12:13]
	s_mov_b32 m0, s28
	s_add_i32 s28, s28, 0x1000
	global_load_lds_dwordx4 v5, s[14:15]
	s_mov_b32 m0, s28
	s_add_i32 s28, s28, 0x1000
	global_load_lds_dwordx4 v6, s[16:17]
	s_mov_b32 m0, s28
	s_add_i32 s28, s28, 0x1000
	global_load_lds_dwordx4 v6, s[18:19]
	s_mov_b32 m0, s28
	s_add_i32 s28, s28, 0x1000
	global_load_lds_dwordx4 v6, s[24:25]
	s_mov_b32 m0, s28
	s_add_i32 s28, s28, 0x1000
	global_load_lds_dwordx4 v6, s[26:27]
	v_add_u32_e32 v5, 196608, v5
	v_add_u32_e32 v6, 262144, v6
	s_add_i32 s31, s29, 1
	s_cmp_lg_u32 s29, 4
	s_cselect_b32 s29, s31, 0
	s_add_i32 s30, s30, -1
	s_cmp_eq_u32 s30, 0
	s_cbranch_scc0 .Lg0_ploop
	s_waitcnt vmcnt(21)
	s_barrier
	s_waitcnt vmcnt(14)
	s_barrier
	s_waitcnt vmcnt(7)
	s_barrier
	s_waitcnt vmcnt(0)
	s_barrier
	s_waitcnt vmcnt(0)
	s_barrier
	s_endpgm
